# gemm: counted vmcnt keeps next-tile DMA in flight; gemm prologue rewritten (one kernarg load, all loads issued together, grid hardcoded); csr gather batched LDS id reads; nt on z load / aggq store
# speedup vs baseline: 1.0224x; 1.0224x over previous
.LBB1_132:
	v_cvt_f32_i32_e32 v8, v50
	v_mov_b32_e32 v9, 0
	v_max_f32_e32 v8, 1.0, v8
	v_rcp_f32_e32 v10, v8
	v_mov_b32_e32 v8, 0
	v_mul_f32_e32 v4, v4, v10
	v_mul_f32_e32 v5, v5, v10
	v_mul_f32_e32 v2, v2, v10
	v_mul_f32_e32 v3, v3, v10
	v_cvt_pk_fp8_f32 v8, v4, v5
	v_cvt_pk_fp8_f32 v9, v2, v3
	v_mul_f32_e32 v6, v6, v10
	v_mul_f32_e32 v7, v7, v10
	v_mul_f32_e32 v0, v0, v10
	v_mul_f32_e32 v1, v1, v10
	v_cvt_pk_fp8_f32 v8, v6, v7 op_sel:[0,0,1]
	v_cvt_pk_fp8_f32 v9, v0, v1 op_sel:[0,0,1]
	v_lshl_or_b32 v0, v49, 4, v44
	v_ashrrev_i32_e32 v1, 31, v0
	v_lshl_add_u64 v[0:1], v[0:1], 3, s[36:37]
	global_store_dwordx2 v[0:1], v[8:9], off nt

.LBB1_145:
	ds_read_u16 v12, v51
	ds_read_u16 v14, v51 offset:2
	ds_read_u16 v22, v51 offset:4
	ds_read_u16 v32, v51 offset:6
	ds_read_u16 v16, v51 offset:8
	ds_read_u16 v28, v51 offset:10
	ds_read_u16 v10, v51 offset:12
	ds_read_u16 v8, v51 offset:14
	s_add_i32 s12, s15, -6
	v_cmp_lt_i32_e64 s[46:47], s12, v50
	s_add_i32 s12, s15, -5
	v_cmp_lt_i32_e64 s[48:49], s12, v50
	s_add_i32 s12, s15, -4
	v_cmp_lt_i32_e64 s[50:51], s12, v50
	s_add_i32 s12, s15, -3
	v_cmp_lt_i32_e64 s[52:53], s12, v50
	s_add_i32 s12, s15, -2
	v_cmp_lt_i32_e64 s[54:55], s12, v50
	s_add_i32 s12, s15, -1
	v_cmp_lt_i32_e64 s[56:57], s12, v50
	v_cmp_lt_i32_e64 s[58:59], s15, v50
	v_mov_b32_e32 v9, 0xc378
	s_waitcnt lgkmcnt(7)
	v_lshl_or_b32 v12, v12, 7, v47
	global_load_dwordx2 v[12:13], v12, s[34:35]
	s_waitcnt lgkmcnt(6)
	v_cndmask_b32_e64 v14, v9, v14, s[46:47]
	v_lshl_or_b32 v14, v14, 7, v47
	global_load_dwordx2 v[14:15], v14, s[34:35]
	s_waitcnt lgkmcnt(5)
	v_cndmask_b32_e64 v22, v9, v22, s[48:49]
	v_lshl_or_b32 v22, v22, 7, v47
	global_load_dwordx2 v[22:23], v22, s[34:35]
	s_waitcnt lgkmcnt(4)
	v_cndmask_b32_e64 v32, v9, v32, s[50:51]
	v_lshl_or_b32 v32, v32, 7, v47
	global_load_dwordx2 v[32:33], v32, s[34:35]
	s_waitcnt lgkmcnt(3)
	v_cndmask_b32_e64 v16, v9, v16, s[52:53]
	v_lshl_or_b32 v16, v16, 7, v47
	global_load_dwordx2 v[16:17], v16, s[34:35]
	s_waitcnt lgkmcnt(2)
	v_cndmask_b32_e64 v28, v9, v28, s[54:55]
	v_lshl_or_b32 v28, v28, 7, v47
	global_load_dwordx2 v[28:29], v28, s[34:35]
	s_waitcnt lgkmcnt(1)
	v_cndmask_b32_e64 v10, v9, v10, s[56:57]
	v_lshl_or_b32 v10, v10, 7, v47
	global_load_dwordx2 v[10:11], v10, s[34:35]
	s_waitcnt lgkmcnt(0)
	v_cndmask_b32_e64 v8, v9, v8, s[58:59]
	v_lshl_or_b32 v8, v8, 7, v47
	global_load_dwordx2 v[8:9], v8, s[34:35]
	s_waitcnt vmcnt(7)
	v_cvt_pk_f32_fp8_e32 v[40:41], v12
	v_cvt_pk_f32_fp8_sdwa v[52:53], v12 src0_sel:WORD_1
	v_cvt_pk_f32_fp8_e32 v[54:55], v13
	v_cvt_pk_f32_fp8_sdwa v[56:57], v13 src0_sel:WORD_1
	s_waitcnt vmcnt(6)
	v_cvt_pk_f32_fp8_e32 v[26:27], v14
	v_cvt_pk_f32_fp8_sdwa v[34:35], v14 src0_sel:WORD_1
	v_cvt_pk_f32_fp8_e32 v[38:39], v15
	v_cvt_pk_f32_fp8_sdwa v[58:59], v15 src0_sel:WORD_1
	s_waitcnt vmcnt(5)
	v_cvt_pk_f32_fp8_e32 v[14:15], v22
	v_cvt_pk_f32_fp8_sdwa v[18:19], v22 src0_sel:WORD_1
	v_cvt_pk_f32_fp8_e32 v[20:21], v23
	v_cvt_pk_f32_fp8_sdwa v[22:23], v23 src0_sel:WORD_1
	s_waitcnt vmcnt(4)
	v_cvt_pk_f32_fp8_e32 v[12:13], v32
	v_cvt_pk_f32_fp8_sdwa v[24:25], v32 src0_sel:WORD_1
	v_cvt_pk_f32_fp8_e32 v[30:31], v33
	v_cvt_pk_f32_fp8_sdwa v[36:37], v33 src0_sel:WORD_1
	s_waitcnt vmcnt(3)
	v_cvt_pk_f32_fp8_e32 v[32:33], v16
	v_pk_add_f32 v[42:43], v[4:5], v[40:41]
	v_cvt_pk_f32_fp8_sdwa v[4:5], v16 src0_sel:WORD_1
	v_pk_add_f32 v[52:53], v[6:7], v[52:53]
	v_cvt_pk_f32_fp8_e32 v[6:7], v17
	v_cvt_pk_f32_fp8_sdwa v[16:17], v17 src0_sel:WORD_1
	v_pk_add_f32 v[54:55], v[2:3], v[54:55]
	v_pk_add_f32 v[40:41], v[0:1], v[56:57]
	s_waitcnt vmcnt(2)
	v_cvt_pk_f32_fp8_e32 v[2:3], v28
	v_cvt_pk_f32_fp8_sdwa v[0:1], v28 src0_sel:WORD_1
	v_pk_add_f32 v[56:57], v[40:41], v[58:59]
	v_cvt_pk_f32_fp8_e32 v[40:41], v29
	v_cvt_pk_f32_fp8_sdwa v[28:29], v29 src0_sel:WORD_1
	v_pk_add_f32 v[38:39], v[54:55], v[38:39]
	v_pk_add_f32 v[34:35], v[52:53], v[34:35]
	v_pk_add_f32 v[26:27], v[42:43], v[26:27]
	s_waitcnt vmcnt(1)
	v_cvt_pk_f32_fp8_e32 v[54:55], v10
	v_cvt_pk_f32_fp8_sdwa v[52:53], v10 src0_sel:WORD_1
	v_cvt_pk_f32_fp8_e32 v[42:43], v11
	v_cvt_pk_f32_fp8_sdwa v[10:11], v11 src0_sel:WORD_1
	v_pk_add_f32 v[14:15], v[26:27], v[14:15]
	v_pk_add_f32 v[18:19], v[34:35], v[18:19]
	v_pk_add_f32 v[20:21], v[38:39], v[20:21]
	v_pk_add_f32 v[22:23], v[56:57], v[22:23]
	v_pk_add_f32 v[20:21], v[20:21], v[30:31]
	v_pk_add_f32 v[22:23], v[22:23], v[36:37]
	v_pk_add_f32 v[18:19], v[18:19], v[24:25]
	v_pk_add_f32 v[12:13], v[14:15], v[12:13]
	v_pk_add_f32 v[4:5], v[18:19], v[4:5]
	v_pk_add_f32 v[12:13], v[12:13], v[32:33]
	v_pk_add_f32 v[6:7], v[20:21], v[6:7]
	v_pk_add_f32 v[14:15], v[22:23], v[16:17]
	v_pk_add_f32 v[6:7], v[6:7], v[40:41]
	v_pk_add_f32 v[14:15], v[14:15], v[28:29]
	v_pk_add_f32 v[0:1], v[4:5], v[0:1]
	v_pk_add_f32 v[2:3], v[12:13], v[2:3]
	v_pk_add_f32 v[12:13], v[0:1], v[52:53]
	v_pk_add_f32 v[4:5], v[2:3], v[54:55]
	v_pk_add_f32 v[2:3], v[6:7], v[42:43]
	v_pk_add_f32 v[0:1], v[14:15], v[10:11]
	s_add_i32 s13, s15, 1
	s_add_i32 s12, s15, 8
	v_cmp_ge_i32_e32 vcc, s13, v50
	v_add_u32_e32 v51, 16, v51
	s_or_b64 s[2:3], vcc, s[2:3]
	s_mov_b32 s15, s12
	s_waitcnt vmcnt(0)
	v_cvt_pk_f32_fp8_sdwa v[6:7], v9 src0_sel:WORD_1
	v_cvt_pk_f32_fp8_e32 v[10:11], v9
	v_cvt_pk_f32_fp8_sdwa v[14:15], v8 src0_sel:WORD_1
	v_cvt_pk_f32_fp8_e32 v[8:9], v8
	v_pk_add_f32 v[0:1], v[0:1], v[6:7]
	v_pk_add_f32 v[2:3], v[2:3], v[10:11]
	v_pk_add_f32 v[6:7], v[12:13], v[14:15]
	v_pk_add_f32 v[4:5], v[4:5], v[8:9]
	s_andn2_b64 exec, exec, s[2:3]
	s_cbranch_execnz .LBB1_145
	s_branch .LBB1_130

	.amdhsa_kernel _Z10k_csr_agg1PKjPKiPiPtPjPK15HIP_vector_typeIjLj2EEPS7_SA_
		.amdhsa_group_segment_fixed_size 25136
		.amdhsa_private_segment_fixed_size 0
		.amdhsa_kernarg_size 64
		.amdhsa_user_sgpr_count 2
		.amdhsa_user_sgpr_dispatch_ptr 0
		.amdhsa_user_sgpr_queue_ptr 0
		.amdhsa_user_sgpr_kernarg_segment_ptr 1
		.amdhsa_user_sgpr_dispatch_id 0
		.amdhsa_user_sgpr_kernarg_preload_length 0
		.amdhsa_user_sgpr_kernarg_preload_offset 0
		.amdhsa_user_sgpr_private_segment_size 0
		.amdhsa_uses_dynamic_stack 0
		.amdhsa_enable_private_segment 0
		.amdhsa_system_sgpr_workgroup_id_x 1
		.amdhsa_system_sgpr_workgroup_id_y 0
		.amdhsa_system_sgpr_workgroup_id_z 0
		.amdhsa_system_sgpr_workgroup_info 0
		.amdhsa_system_vgpr_workitem_id 0
		.amdhsa_next_free_vgpr 60
		.amdhsa_next_free_sgpr 60
		.amdhsa_accum_offset 60
		.amdhsa_reserve_vcc 1
		.amdhsa_float_round_mode_32 0
		.amdhsa_float_round_mode_16_64 0
		.amdhsa_float_denorm_mode_32 3
		.amdhsa_float_denorm_mode_16_64 3
		.amdhsa_dx10_clamp 1
		.amdhsa_ieee_mode 1
		.amdhsa_fp16_overflow 0
		.amdhsa_tg_split 0
		.amdhsa_exception_fp_ieee_invalid_op 0
		.amdhsa_exception_fp_denorm_src 0
		.amdhsa_exception_fp_ieee_div_zero 0
		.amdhsa_exception_fp_ieee_overflow 0
		.amdhsa_exception_fp_ieee_underflow 0
		.amdhsa_exception_fp_ieee_inexact 0
		.amdhsa_exception_int_div_zero 0
	.end_amdhsa_kernel

_Z6k_gemmPK15HIP_vector_typeIjLj4EES2_PKS_IjLj2EES5_PKfS7_S7_PjS8_:
	s_load_dwordx16 s[32:47], s[0:1], 0x0
	s_load_dwordx2 s[10:11], s[0:1], 0x40
	v_and_b32_e32 v4, 63, v0
	v_lshrrev_b32_e32 v94, 6, v0
	v_and_b32_e32 v1, 31, v0
	s_movk_i32 s3, 0xff
	v_cmp_lt_u32_e64 s[6:7], s3, v0
	s_movk_i32 s3, 0x100
	v_cmp_gt_u32_e64 s[4:5], s3, v0
	v_lshlrev_b32_e32 v98, 10, v94
	v_lshlrev_b32_e32 v5, 5, v4
	v_lshl_or_b32 v2, v94, 13, v5
	v_mov_b32_e32 v3, 0
	v_mov_b32_e32 v29, 0
	v_mov_b32_e32 v9, 0
	v_mov_b32_e32 v31, 0
	v_and_b32_e32 v8, 32, v4
	v_bfe_u32 v10, v0, 6, 1
	v_lshlrev_b32_e32 v30, 4, v10
	v_lshrrev_b32_e32 v5, 5, v0
	v_and_b32_e32 v5, 4, v5
	v_lshlrev_b32_e32 v28, 4, v5
	s_lshl_b32 s16, s2, 6
	s_lshl_b32 s17, s2, 1
	v_or_b32_e32 v5, s16, v1
	v_min_i32_e32 v5, 0xc34f, v5
	v_lshlrev_b32_e32 v6, 4, v5
	v_ashrrev_i32_e32 v7, 31, v6
	s_or_b32 s12, s17, 1
	s_min_i32 s12, s12, 0x61b
	v_lshl_or_b32 v5, s12, 5, v1
	v_min_i32_e32 v5, 0xc34f, v5
	v_lshlrev_b32_e32 v100, 4, v5
	v_ashrrev_i32_e32 v101, 31, v100
	v_readfirstlane_b32 s13, v98
	v_or_b32_e32 v5, 0x2000, v98
	s_movk_i32 s3, 0x200
	s_sub_i32 s18, 0x50d, s2
	s_lshr_b32 s18, s18, 9
	s_mov_b32 s15, 0
	v_readfirstlane_b32 s19, v5
	s_waitcnt lgkmcnt(0)
	v_mov_b32_e32 v26, s38
	v_mov_b32_e32 v27, s39
	v_mov_b32_e32 v102, s36
	v_mov_b32_e32 v103, s37
	v_cndmask_b32_e64 v26, v26, v102, s[4:5]
	v_cndmask_b32_e64 v27, v27, v103, s[4:5]
	s_mov_b64 s[8:9], s[46:47]
	v_lshl_add_u64 v[6:7], v[6:7], 3, v[26:27]
	v_lshl_add_u64 v[100:101], v[100:101], 3, v[26:27]
	v_lshl_add_u64 v[6:7], v[6:7], 0, v[28:29]
	v_lshl_add_u64 v[100:101], v[100:101], 0, v[28:29]
	v_lshl_add_u64 v[6:7], v[6:7], 0, v[8:9]
	v_lshl_add_u64 v[100:101], v[100:101], 0, v[8:9]
	s_mov_b32 m0, s13
	v_lshl_add_u64 v[6:7], v[6:7], 0, v[30:31]
	v_lshl_add_u64 v[100:101], v[100:101], 0, v[30:31]
	global_load_lds_dwordx4 v[6:7], off
	global_load_dwordx4 v[34:37], v2, s[34:35]
	global_load_dwordx4 v[38:41], v2, s[34:35] offset:16
	s_mov_b32 m0, s19
	v_or_b32_e32 v5, 0x1000, v2
	global_load_lds_dwordx4 v[100:101], off
	global_load_dwordx4 v[50:53], v2, s[34:35] offset:2048
	global_load_dwordx4 v[54:57], v2, s[34:35] offset:2064
	global_load_dwordx4 v[66:69], v5, s[34:35]
	global_load_dwordx4 v[70:73], v5, s[34:35] offset:16
	global_load_dwordx4 v[42:45], v2, s[32:33]
	global_load_dwordx4 v[46:49], v2, s[32:33] offset:16
	global_load_dwordx4 v[58:61], v2, s[32:33] offset:2048
	global_load_dwordx4 v[62:65], v2, s[32:33] offset:2064
	global_load_dwordx4 v[74:77], v5, s[32:33]
	global_load_dwordx4 v[78:81], v5, s[32:33] offset:16
	global_load_dwordx4 v[82:85], v5, s[32:33] offset:2048
	global_load_dwordx4 v[86:89], v5, s[32:33] offset:2064
	v_lshlrev_b32_e32 v104, 1, v0
	v_lshrrev_b32_e32 v105, 2, v0
	v_and_b32_e32 v106, 0xe3, v0
	v_and_b32_e32 v104, 24, v104
	v_and_b32_e32 v105, 4, v105
	v_or3_b32 v106, v104, v106, v105
	v_lshlrev_b32_e32 v106, 2, v106
	v_mov_b32_e32 v107, 0x12300
	v_lshl_add_u32 v107, v0, 2, v107
	v_lshl_add_u64 v[2:3], s[34:35], 0, v[2:3]
	s_and_saveexec_b64 s[12:13], s[4:5]
	s_cbranch_execz .Lg_pro_nobias
	global_load_dword v108, v106, s[40:41]
	global_load_dword v109, v106, s[44:45]
	v_mov_b32_e32 v110, 0
	s_movk_i32 s0, 0x7f
	v_cmp_lt_u32_e32 vcc, s0, v0
	s_and_saveexec_b64 s[20:21], vcc
	s_cbranch_execz .Lg_pro_nob2
	global_load_dword v110, v106, s[42:43] offset:-512
.Lg_pro_nob2:
	s_or_b64 exec, exec, s[20:21]
	s_waitcnt vmcnt(0)
	ds_write_b32 v107, v108
	v_fmac_f32_e32 v110, 0.5, v109
	ds_write_b32 v107, v110 offset:1024
.Lg_pro_nobias:
	s_or_b64 exec, exec, s[12:13]
	s_waitcnt vmcnt(0)
	s_sub_i32 s14, s18, s15
	s_cmp_lt_i32 s14, 1
	s_cbranch_scc1 .LBB2_40
	s_mov_b64 s[0:1], 0x1800
	v_lshl_add_u64 v[90:91], v[2:3], 0, s[0:1]
	s_movk_i32 s0, 0x1000
	v_add_co_u32_e32 v2, vcc, s0, v2
	s_waitcnt lgkmcnt(0)
	s_barrier
	s_nop 0
	v_addc_co_u32_e32 v3, vcc, 0, v3, vcc
	global_load_dwordx4 v[18:21], v[2:3], off offset:2048
	global_load_dwordx4 v[22:25], v[90:91], off offset:16
	v_lshrrev_b32_e32 v95, 5, v4
	v_mov_b32_e32 v5, 0x12300
	v_lshl_add_u32 v32, v94, 7, v5
	v_lshlrev_b32_e32 v33, 6, v95
	v_or_b32_e32 v14, v32, v33
	v_lshlrev_b32_e32 v99, 4, v4
	ds_read_b128 v[2:5], v14
	ds_read_b128 v[6:9], v14 offset:16
	ds_read_b128 v[10:13], v14 offset:32
	ds_read_b128 v[14:17], v14 offset:48
	s_nop 0
	ds_read_b128 v[100:103], v99
	ds_read_b128 v[104:107], v99 offset:1024
	v_mov_b32_e32 v96, 0x7f7f7f7f
	v_lshlrev_b32_e32 v92, 1, v95
	v_lshl_add_u64 v[26:27], v[26:27], 0, v[28:29]
	s_waitcnt lgkmcnt(0)
	v_mfma_scale_f32_32x32x64_f8f6f4 v[2:17], v[34:41], v[100:107], v[2:17], v96, v96 op_sel_hi:[0,0,0]
	v_lshlrev_b32_e32 v28, 4, v92
	s_cmpk_lt_i32 s2, 0x30d
	v_lshl_add_u64 v[26:27], v[26:27], 0, v[28:29]
	s_cselect_b64 s[0:1], -1, 0
	s_add_i32 s12, s3, s2
	v_lshl_add_u64 v[92:93], v[26:27], 0, v[30:31]
	v_lshl_or_b32 v26, s12, 6, v1
	v_min_i32_e32 v26, 0xc34f, v26
	s_lshl_b32 s13, s12, 1
	v_lshlrev_b32_e32 v26, 4, v26
	v_or_b32_e32 v28, 0x4000, v98
	s_or_b32 s13, s13, 1
	v_ashrrev_i32_e32 v27, 31, v26
	v_readfirstlane_b32 s12, v28
	s_min_i32 s13, s13, 0x61b
	v_lshl_add_u64 v[26:27], v[26:27], 3, v[92:93]
	s_mov_b32 m0, s12
	ds_read_b128 v[100:103], v99 offset:2048
	ds_read_b128 v[104:107], v99 offset:3072
	global_load_lds_dwordx4 v[26:27], off
	v_lshl_or_b32 v26, s13, 5, v1
	v_min_i32_e32 v26, 0xc34f, v26
	v_lshlrev_b32_e32 v26, 4, v26
	v_or_b32_e32 v28, 0x6000, v98
	v_ashrrev_i32_e32 v27, 31, v26
	v_readfirstlane_b32 s12, v28
	v_lshl_add_u64 v[26:27], v[26:27], 3, v[92:93]
	s_mov_b32 m0, s12
	s_waitcnt lgkmcnt(0)
	v_mfma_scale_f32_32x32x64_f8f6f4 v[2:17], v[50:57], v[100:107], v[2:17], v96, v96 op_sel_hi:[0,0,0]
	s_nop 0
	ds_read_b128 v[100:103], v99 offset:4096
	ds_read_b128 v[104:107], v99 offset:5120
	global_load_lds_dwordx4 v[26:27], off
	v_mov_b32_e32 v26, v29
	s_cmpk_gt_i32 s2, 0x30c
	s_waitcnt lgkmcnt(0)
	v_mfma_scale_f32_32x32x64_f8f6f4 v[2:17], v[66:73], v[100:107], v[2:17], v96, v96 op_sel_hi:[0,0,0]
	s_waitcnt vmcnt(2)
	ds_read_b128 v[100:103], v99 offset:6144
	ds_read_b128 v[104:107], v99 offset:7168
	s_waitcnt lgkmcnt(0)
	v_mfma_scale_f32_32x32x64_f8f6f4 v[2:17], v[18:25], v[100:107], v[2:17], v96, v96 op_sel_hi:[0,0,0]
	s_nop 15
	s_nop 3
	v_mul_f32_e32 v2, 0xbfb8aa3b, v2
	v_mul_f32_e32 v3, 0xbfb8aa3b, v3
	v_exp_f32_e32 v2, v2
	v_exp_f32_e32 v3, v3
	v_mul_f32_e32 v4, 0xbfb8aa3b, v4
	v_mul_f32_e32 v5, 0xbfb8aa3b, v5
	v_exp_f32_e32 v4, v4
	v_exp_f32_e32 v5, v5
	v_add_f32_e32 v2, 1.0, v2
	v_add_f32_e32 v3, 1.0, v3
	v_rcp_f32_e32 v2, v2
	v_rcp_f32_e32 v3, v3
	v_add_f32_e32 v4, 1.0, v4
	v_add_f32_e32 v5, 1.0, v5
	v_rcp_f32_e32 v4, v4
	v_rcp_f32_e32 v5, v5
	v_add_f32_e32 v2, -0.5, v2
	v_add_f32_e32 v3, -0.5, v3
	v_cvt_pk_fp8_f32 v26, v2, v3
	v_add_f32_e32 v2, -0.5, v4
	v_add_f32_e32 v3, -0.5, v5
	v_cvt_pk_fp8_f32 v26, v2, v3 op_sel:[0,0,1]
	v_or_b32_e32 v2, 0x8000, v98
	v_add_u32_e32 v100, v2, v99
	v_mul_f32_e32 v2, 0xbfb8aa3b, v6
	v_mul_f32_e32 v3, 0xbfb8aa3b, v7
	v_exp_f32_e32 v2, v2
	v_exp_f32_e32 v3, v3
	v_mul_f32_e32 v4, 0xbfb8aa3b, v8
	v_mul_f32_e32 v5, 0xbfb8aa3b, v9
	v_add_f32_e32 v2, 1.0, v2
	v_exp_f32_e32 v4, v4
	v_add_f32_e32 v3, 1.0, v3
	v_exp_f32_e32 v5, v5
	v_rcp_f32_e32 v2, v2
	v_rcp_f32_e32 v3, v3
	v_add_f32_e32 v4, 1.0, v4
	v_add_f32_e32 v5, 1.0, v5
	v_add_f32_e32 v2, -0.5, v2
	v_add_f32_e32 v3, -0.5, v3
	v_rcp_f32_e32 v4, v4
	v_rcp_f32_e32 v5, v5
	v_mov_b32_e32 v27, v29
	v_cvt_pk_fp8_f32 v27, v2, v3
	v_add_f32_e32 v2, -0.5, v4
	v_add_f32_e32 v3, -0.5, v5
	v_cvt_pk_fp8_f32 v27, v2, v3 op_sel:[0,0,1]
	v_mul_f32_e32 v2, 0xbfb8aa3b, v10
	v_mul_f32_e32 v3, 0xbfb8aa3b, v11
	v_exp_f32_e32 v2, v2
	v_exp_f32_e32 v3, v3
	v_mul_f32_e32 v4, 0xbfb8aa3b, v12
	v_mul_f32_e32 v5, 0xbfb8aa3b, v13
	v_add_f32_e32 v2, 1.0, v2
	v_exp_f32_e32 v4, v4
	v_add_f32_e32 v3, 1.0, v3
	v_exp_f32_e32 v5, v5
	v_rcp_f32_e32 v2, v2
	v_rcp_f32_e32 v3, v3
	v_add_f32_e32 v4, 1.0, v4
	v_add_f32_e32 v5, 1.0, v5
	v_add_f32_e32 v2, -0.5, v2
	v_add_f32_e32 v3, -0.5, v3
	v_rcp_f32_e32 v4, v4
	v_rcp_f32_e32 v5, v5
	v_mov_b32_e32 v28, v29
	v_cvt_pk_fp8_f32 v28, v2, v3
	v_add_f32_e32 v2, -0.5, v4
	v_add_f32_e32 v3, -0.5, v5
	v_cvt_pk_fp8_f32 v28, v2, v3 op_sel:[0,0,1]
	v_mul_f32_e32 v2, 0xbfb8aa3b, v14
	v_mul_f32_e32 v3, 0xbfb8aa3b, v15
	v_exp_f32_e32 v2, v2
	v_exp_f32_e32 v3, v3
	v_mul_f32_e32 v4, 0xbfb8aa3b, v16
	v_mul_f32_e32 v5, 0xbfb8aa3b, v17
	v_add_f32_e32 v2, 1.0, v2
	v_exp_f32_e32 v4, v4
	v_add_f32_e32 v3, 1.0, v3
	v_exp_f32_e32 v5, v5
	v_rcp_f32_e32 v2, v2
	v_rcp_f32_e32 v3, v3
	v_add_f32_e32 v4, 1.0, v4
	v_add_f32_e32 v5, 1.0, v5
	v_add_f32_e32 v2, -0.5, v2
	v_add_f32_e32 v3, -0.5, v3
	v_rcp_f32_e32 v4, v4
	v_rcp_f32_e32 v5, v5
	v_cvt_pk_fp8_f32 v29, v2, v3
	v_add_f32_e32 v2, -0.5, v4
	v_add_f32_e32 v3, -0.5, v5
	v_cvt_pk_fp8_f32 v29, v2, v3 op_sel:[0,0,1]
	v_add_u32_e32 v101, v32, v33
	ds_write_b128 v100, v[26:29]
	s_cbranch_scc1 .LBB2_7
	ds_read_b128 v[2:5], v101
	ds_read_b128 v[6:9], v101 offset:16
	ds_read_b128 v[10:13], v101 offset:32
	ds_read_b128 v[14:17], v101 offset:48
	ds_read_b128 v[26:29], v99 offset:8192
	ds_read_b128 v[30:33], v99 offset:9216
	s_waitcnt lgkmcnt(0)
	v_mfma_scale_f32_32x32x64_f8f6f4 v[2:17], v[34:41], v[26:33], v[2:17], v96, v96 op_sel_hi:[0,0,0]
	ds_read_b128 v[26:29], v99 offset:10240
	ds_read_b128 v[30:33], v99 offset:11264
	s_waitcnt lgkmcnt(0)
	v_mfma_scale_f32_32x32x64_f8f6f4 v[2:17], v[50:57], v[26:33], v[2:17], v96, v96 op_sel_hi:[0,0,0]
	ds_read_b128 v[26:29], v99 offset:12288
	ds_read_b128 v[30:33], v99 offset:13312
	s_waitcnt lgkmcnt(0)
	v_mfma_scale_f32_32x32x64_f8f6f4 v[2:17], v[66:73], v[26:33], v[2:17], v96, v96 op_sel_hi:[0,0,0]
	ds_read_b128 v[26:29], v99 offset:14336
	ds_read_b128 v[30:33], v99 offset:15360
	s_waitcnt lgkmcnt(0)
	v_mfma_scale_f32_32x32x64_f8f6f4 v[2:17], v[18:25], v[26:33], v[2:17], v96, v96 op_sel_hi:[0,0,0]
	s_nop 15
	s_nop 3
	v_mul_f32_e32 v2, 0xbfb8aa3b, v2
	v_mul_f32_e32 v3, 0xbfb8aa3b, v3
	v_exp_f32_e32 v2, v2
	v_exp_f32_e32 v3, v3
	v_mul_f32_e32 v4, 0xbfb8aa3b, v4
	v_mul_f32_e32 v5, 0xbfb8aa3b, v5
	v_exp_f32_e32 v4, v4
	v_exp_f32_e32 v5, v5
	v_add_f32_e32 v2, 1.0, v2
	v_add_f32_e32 v3, 1.0, v3
	v_rcp_f32_e32 v2, v2
	v_rcp_f32_e32 v3, v3
	v_add_f32_e32 v4, 1.0, v4
	v_add_f32_e32 v5, 1.0, v5
	v_rcp_f32_e32 v4, v4
	v_rcp_f32_e32 v5, v5
	v_add_f32_e32 v18, -0.5, v2
	v_add_f32_e32 v3, -0.5, v3
	v_mov_b32_e32 v2, 0
	v_cvt_pk_fp8_f32 v2, v18, v3
	v_add_f32_e32 v3, -0.5, v4
	v_add_f32_e32 v4, -0.5, v5
	v_mov_b32_e32 v5, 0
	v_cvt_pk_fp8_f32 v2, v3, v4 op_sel:[0,0,1]
	v_mul_f32_e32 v3, 0xbfb8aa3b, v6
	v_exp_f32_e32 v3, v3
	v_mul_f32_e32 v4, 0xbfb8aa3b, v7
	v_exp_f32_e32 v4, v4
	v_mul_f32_e32 v6, 0xbfb8aa3b, v8
	v_add_f32_e32 v3, 1.0, v3
	v_rcp_f32_e32 v3, v3
	v_exp_f32_e32 v6, v6
	v_add_f32_e32 v4, 1.0, v4
	v_rcp_f32_e32 v4, v4
	v_add_f32_e32 v7, -0.5, v3
	v_mul_f32_e32 v3, 0xbfb8aa3b, v9
	v_exp_f32_e32 v3, v3
	v_add_f32_e32 v6, 1.0, v6
	v_add_f32_e32 v4, -0.5, v4
	v_rcp_f32_e32 v6, v6
	v_add_f32_e32 v3, 1.0, v3
	v_rcp_f32_e32 v8, v3
	v_mov_b32_e32 v3, 0
	v_cvt_pk_fp8_f32 v3, v7, v4
	v_add_f32_e32 v4, -0.5, v6
	v_add_f32_e32 v6, -0.5, v8
	v_cvt_pk_fp8_f32 v3, v4, v6 op_sel:[0,0,1]
	v_mul_f32_e32 v4, 0xbfb8aa3b, v10
	v_exp_f32_e32 v4, v4
	v_mul_f32_e32 v6, 0xbfb8aa3b, v11
	v_exp_f32_e32 v6, v6
	v_mul_f32_e32 v7, 0xbfb8aa3b, v12
	v_add_f32_e32 v4, 1.0, v4
	v_rcp_f32_e32 v4, v4
	v_exp_f32_e32 v7, v7
	v_add_f32_e32 v6, 1.0, v6
	v_rcp_f32_e32 v6, v6
	v_add_f32_e32 v8, -0.5, v4
	v_mul_f32_e32 v4, 0xbfb8aa3b, v13
	v_exp_f32_e32 v4, v4
	v_add_f32_e32 v7, 1.0, v7
	v_add_f32_e32 v6, -0.5, v6
	v_rcp_f32_e32 v7, v7
	v_add_f32_e32 v4, 1.0, v4
	v_rcp_f32_e32 v9, v4
	v_mov_b32_e32 v4, 0
	v_cvt_pk_fp8_f32 v4, v8, v6
	v_add_f32_e32 v6, -0.5, v7
	v_add_f32_e32 v7, -0.5, v9
	v_cvt_pk_fp8_f32 v4, v6, v7 op_sel:[0,0,1]
	v_mul_f32_e32 v6, 0xbfb8aa3b, v14
	v_mul_f32_e32 v7, 0xbfb8aa3b, v15
	v_exp_f32_e32 v6, v6
	v_exp_f32_e32 v7, v7
	v_mul_f32_e32 v8, 0xbfb8aa3b, v16
	v_mul_f32_e32 v9, 0xbfb8aa3b, v17
	v_add_f32_e32 v6, 1.0, v6
	v_exp_f32_e32 v8, v8
	v_add_f32_e32 v7, 1.0, v7
	v_exp_f32_e32 v9, v9
	v_rcp_f32_e32 v6, v6
	v_rcp_f32_e32 v7, v7
	v_add_f32_e32 v8, 1.0, v8
	v_add_f32_e32 v9, 1.0, v9
	v_add_f32_e32 v6, -0.5, v6
	v_add_f32_e32 v7, -0.5, v7
	v_rcp_f32_e32 v8, v8
	v_rcp_f32_e32 v9, v9
	v_cvt_pk_fp8_f32 v5, v6, v7
	v_add_f32_e32 v6, -0.5, v8
	v_add_f32_e32 v7, -0.5, v9
	v_cvt_pk_fp8_f32 v5, v6, v7 op_sel:[0,0,1]
	ds_write_b128 v100, v[2:5] offset:8192

.LBB2_29:
	s_add_i32 s23, s3, s23
	s_cmpk_lt_i32 s23, 0x30d
	s_cselect_b64 s[0:1], -1, 0
	s_xor_b32 s24, s12, 1
	v_min_i32_e32 v2, 0xc34f, v107
	v_lshlrev_b32_e32 v2, 4, v2
	v_lshl_or_b32 v4, s24, 14, v98
	s_add_i32 s13, s18, s17
	v_ashrrev_i32_e32 v3, 31, v2
	v_readfirstlane_b32 s25, v4
	s_min_i32 s13, s13, 0x61b
	v_lshl_add_u64 v[2:3], v[2:3], 3, v[92:93]
	s_mov_b32 m0, s25
	v_or_b32_e32 v4, 0x2000, v4
	global_load_lds_dwordx4 v[2:3], off
	v_lshl_or_b32 v2, s13, 5, v1
	v_min_i32_e32 v2, 0xc34f, v2
	v_lshlrev_b32_e32 v2, 4, v2
	v_ashrrev_i32_e32 v3, 31, v2
	v_readfirstlane_b32 s13, v4
	s_lshl_b32 s12, s12, 14
	v_lshl_add_u64 v[2:3], v[2:3], 3, v[92:93]
	s_mov_b32 m0, s13
	v_or_b32_e32 v95, s12, v99
	global_load_lds_dwordx4 v[2:3], off
	ds_read_b128 v[2:5], v101
	ds_read_b128 v[6:9], v101 offset:16
	ds_read_b128 v[10:13], v101 offset:32
	ds_read_b128 v[14:17], v101 offset:48
	s_waitcnt vmcnt(2)
	ds_read_b128 v[26:29], v95
	ds_read_b128 v[30:33], v95 offset:1024
	s_waitcnt lgkmcnt(0)
	v_mfma_scale_f32_32x32x64_f8f6f4 v[2:17], v[34:41], v[26:33], v[2:17], v110, v110 op_sel_hi:[0,0,0]
	ds_read_b128 v[26:29], v95 offset:2048
	ds_read_b128 v[30:33], v95 offset:3072
	s_cmpk_gt_i32 s23, 0x30c
	s_waitcnt lgkmcnt(0)
	v_mfma_scale_f32_32x32x64_f8f6f4 v[2:17], v[50:57], v[26:33], v[2:17], v110, v110 op_sel_hi:[0,0,0]
	ds_read_b128 v[26:29], v95 offset:4096
	ds_read_b128 v[30:33], v95 offset:5120
	s_waitcnt lgkmcnt(0)
	v_mfma_scale_f32_32x32x64_f8f6f4 v[2:17], v[66:73], v[26:33], v[2:17], v110, v110 op_sel_hi:[0,0,0]
	ds_read_b128 v[26:29], v95 offset:6144
	ds_read_b128 v[30:33], v95 offset:7168
	s_waitcnt lgkmcnt(0)
	v_mfma_scale_f32_32x32x64_f8f6f4 v[2:17], v[18:25], v[26:33], v[2:17], v110, v110 op_sel_hi:[0,0,0]
	s_nop 15
	s_nop 3
	v_mul_f32_e32 v2, 0xbfb8aa3b, v2
	v_mul_f32_e32 v3, 0xbfb8aa3b, v3
	v_exp_f32_e32 v2, v2
	v_exp_f32_e32 v3, v3
	v_mul_f32_e32 v4, 0xbfb8aa3b, v4
	v_mul_f32_e32 v5, 0xbfb8aa3b, v5
	v_exp_f32_e32 v4, v4
	v_exp_f32_e32 v5, v5
	v_add_f32_e32 v2, 1.0, v2
	v_add_f32_e32 v3, 1.0, v3
	v_rcp_f32_e32 v2, v2
	v_rcp_f32_e32 v3, v3
	v_add_f32_e32 v4, 1.0, v4
	v_add_f32_e32 v5, 1.0, v5
	v_rcp_f32_e32 v4, v4
	v_rcp_f32_e32 v5, v5
	v_add_f32_e32 v26, -0.5, v2
	v_add_f32_e32 v3, -0.5, v3
	v_mov_b32_e32 v2, 0
	v_cvt_pk_fp8_f32 v2, v26, v3
	v_add_f32_e32 v3, -0.5, v4
	v_add_f32_e32 v4, -0.5, v5
	v_cvt_pk_fp8_f32 v2, v3, v4 op_sel:[0,0,1]
	v_mul_f32_e32 v3, 0xbfb8aa3b, v6
	v_exp_f32_e32 v3, v3
	v_mul_f32_e32 v4, 0xbfb8aa3b, v7
	v_exp_f32_e32 v4, v4
	v_mul_f32_e32 v5, 0xbfb8aa3b, v8
	v_add_f32_e32 v3, 1.0, v3
	v_rcp_f32_e32 v3, v3
	v_exp_f32_e32 v5, v5
	v_add_f32_e32 v4, 1.0, v4
	v_rcp_f32_e32 v4, v4
	v_add_f32_e32 v6, -0.5, v3
	v_mul_f32_e32 v3, 0xbfb8aa3b, v9
	v_exp_f32_e32 v3, v3
	v_add_f32_e32 v5, 1.0, v5
	v_add_f32_e32 v4, -0.5, v4
	v_rcp_f32_e32 v5, v5
	v_add_f32_e32 v3, 1.0, v3
	v_rcp_f32_e32 v7, v3
	v_mov_b32_e32 v3, 0
	v_cvt_pk_fp8_f32 v3, v6, v4
	v_add_f32_e32 v4, -0.5, v5
	v_add_f32_e32 v5, -0.5, v7
	v_cvt_pk_fp8_f32 v3, v4, v5 op_sel:[0,0,1]
	v_mul_f32_e32 v4, 0xbfb8aa3b, v10
	v_exp_f32_e32 v4, v4
	v_mul_f32_e32 v5, 0xbfb8aa3b, v11
	v_exp_f32_e32 v5, v5
	v_mul_f32_e32 v6, 0xbfb8aa3b, v12
	v_add_f32_e32 v4, 1.0, v4
	v_rcp_f32_e32 v4, v4
	v_exp_f32_e32 v6, v6
	v_add_f32_e32 v5, 1.0, v5
	v_rcp_f32_e32 v5, v5
	v_add_f32_e32 v7, -0.5, v4
	v_mul_f32_e32 v4, 0xbfb8aa3b, v13
	v_exp_f32_e32 v4, v4
	v_add_f32_e32 v6, 1.0, v6
	v_add_f32_e32 v5, -0.5, v5
	v_rcp_f32_e32 v6, v6
	v_add_f32_e32 v4, 1.0, v4
	v_rcp_f32_e32 v8, v4
	v_mov_b32_e32 v4, 0
	v_cvt_pk_fp8_f32 v4, v7, v5
	v_add_f32_e32 v5, -0.5, v6
	v_add_f32_e32 v6, -0.5, v8
	v_cvt_pk_fp8_f32 v4, v5, v6 op_sel:[0,0,1]
	v_mul_f32_e32 v5, 0xbfb8aa3b, v14
	v_exp_f32_e32 v5, v5
	v_mul_f32_e32 v6, 0xbfb8aa3b, v15
	v_exp_f32_e32 v6, v6
	v_mul_f32_e32 v7, 0xbfb8aa3b, v16
	v_add_f32_e32 v5, 1.0, v5
	v_rcp_f32_e32 v5, v5
	v_exp_f32_e32 v7, v7
	v_add_f32_e32 v6, 1.0, v6
	v_rcp_f32_e32 v6, v6
	v_add_f32_e32 v8, -0.5, v5
	v_mul_f32_e32 v5, 0xbfb8aa3b, v17
	v_exp_f32_e32 v5, v5
	v_add_f32_e32 v7, 1.0, v7
	v_add_f32_e32 v6, -0.5, v6
	v_rcp_f32_e32 v7, v7
	v_add_f32_e32 v5, 1.0, v5
	v_rcp_f32_e32 v9, v5
	v_mov_b32_e32 v5, 0
	v_cvt_pk_fp8_f32 v5, v8, v6
	v_add_f32_e32 v6, -0.5, v7
	v_add_f32_e32 v7, -0.5, v9
	v_cvt_pk_fp8_f32 v5, v6, v7 op_sel:[0,0,1]
	ds_write_b128 v100, v[2:5]
	s_cbranch_scc1 .LBB2_31
	v_add_u32_e32 v95, s12, v99
	ds_read_b128 v[2:5], v101
	ds_read_b128 v[6:9], v101 offset:16
	ds_read_b128 v[10:13], v101 offset:32
	ds_read_b128 v[14:17], v101 offset:48
	ds_read_b128 v[26:29], v95 offset:8192
	ds_read_b128 v[30:33], v95 offset:9216
	s_waitcnt lgkmcnt(0)
	v_mfma_scale_f32_32x32x64_f8f6f4 v[2:17], v[34:41], v[26:33], v[2:17], v110, v110 op_sel_hi:[0,0,0]
	ds_read_b128 v[26:29], v95 offset:10240
	ds_read_b128 v[30:33], v95 offset:11264
	s_waitcnt lgkmcnt(0)
	v_mfma_scale_f32_32x32x64_f8f6f4 v[2:17], v[50:57], v[26:33], v[2:17], v110, v110 op_sel_hi:[0,0,0]
	ds_read_b128 v[26:29], v95 offset:12288
	ds_read_b128 v[30:33], v95 offset:13312
	s_waitcnt lgkmcnt(0)
	v_mfma_scale_f32_32x32x64_f8f6f4 v[2:17], v[66:73], v[26:33], v[2:17], v110, v110 op_sel_hi:[0,0,0]
	ds_read_b128 v[26:29], v95 offset:14336
	ds_read_b128 v[30:33], v95 offset:15360
	s_waitcnt lgkmcnt(0)
	v_mfma_scale_f32_32x32x64_f8f6f4 v[2:17], v[18:25], v[26:33], v[2:17], v110, v110 op_sel_hi:[0,0,0]
	s_nop 15
	s_nop 3
	v_mul_f32_e32 v2, 0xbfb8aa3b, v2
	v_mul_f32_e32 v3, 0xbfb8aa3b, v3
	v_exp_f32_e32 v2, v2
	v_exp_f32_e32 v3, v3
	v_mul_f32_e32 v4, 0xbfb8aa3b, v4
	v_mul_f32_e32 v5, 0xbfb8aa3b, v5
	v_exp_f32_e32 v4, v4
	v_exp_f32_e32 v5, v5
	v_add_f32_e32 v2, 1.0, v2
	v_add_f32_e32 v3, 1.0, v3
	v_rcp_f32_e32 v2, v2
	v_rcp_f32_e32 v3, v3
	v_add_f32_e32 v4, 1.0, v4
	v_add_f32_e32 v5, 1.0, v5
	v_rcp_f32_e32 v4, v4
	v_rcp_f32_e32 v5, v5
	v_add_f32_e32 v18, -0.5, v2
	v_add_f32_e32 v3, -0.5, v3
	v_mov_b32_e32 v2, 0
	v_cvt_pk_fp8_f32 v2, v18, v3
	v_add_f32_e32 v3, -0.5, v4
	v_add_f32_e32 v4, -0.5, v5
	v_cvt_pk_fp8_f32 v2, v3, v4 op_sel:[0,0,1]
	v_mul_f32_e32 v3, 0xbfb8aa3b, v6
	v_exp_f32_e32 v3, v3
	v_mul_f32_e32 v4, 0xbfb8aa3b, v7
	v_exp_f32_e32 v4, v4
	v_mul_f32_e32 v5, 0xbfb8aa3b, v8
	v_add_f32_e32 v3, 1.0, v3
	v_rcp_f32_e32 v3, v3
	v_exp_f32_e32 v5, v5
	v_add_f32_e32 v4, 1.0, v4
	v_rcp_f32_e32 v4, v4
	v_add_f32_e32 v6, -0.5, v3
	v_mul_f32_e32 v3, 0xbfb8aa3b, v9
	v_exp_f32_e32 v3, v3
	v_add_f32_e32 v5, 1.0, v5
	v_add_f32_e32 v4, -0.5, v4
	v_rcp_f32_e32 v5, v5
	v_add_f32_e32 v3, 1.0, v3
	v_rcp_f32_e32 v7, v3
	v_mov_b32_e32 v3, 0
	v_cvt_pk_fp8_f32 v3, v6, v4
	v_add_f32_e32 v4, -0.5, v5
	v_add_f32_e32 v5, -0.5, v7
	v_cvt_pk_fp8_f32 v3, v4, v5 op_sel:[0,0,1]
	v_mul_f32_e32 v4, 0xbfb8aa3b, v10
	v_exp_f32_e32 v4, v4
	v_mul_f32_e32 v5, 0xbfb8aa3b, v11
	v_exp_f32_e32 v5, v5
	v_mul_f32_e32 v6, 0xbfb8aa3b, v12
	v_add_f32_e32 v4, 1.0, v4
	v_rcp_f32_e32 v4, v4
	v_exp_f32_e32 v6, v6
	v_add_f32_e32 v5, 1.0, v5
	v_rcp_f32_e32 v5, v5
	v_add_f32_e32 v7, -0.5, v4
	v_mul_f32_e32 v4, 0xbfb8aa3b, v13
	v_exp_f32_e32 v4, v4
	v_add_f32_e32 v6, 1.0, v6
	v_add_f32_e32 v5, -0.5, v5
	v_rcp_f32_e32 v6, v6
	v_add_f32_e32 v4, 1.0, v4
	v_rcp_f32_e32 v8, v4
	v_mov_b32_e32 v4, 0
	v_cvt_pk_fp8_f32 v4, v7, v5
	v_add_f32_e32 v5, -0.5, v6
	v_add_f32_e32 v6, -0.5, v8
	v_cvt_pk_fp8_f32 v4, v5, v6 op_sel:[0,0,1]
	v_mul_f32_e32 v5, 0xbfb8aa3b, v14
	v_exp_f32_e32 v5, v5
	v_mul_f32_e32 v6, 0xbfb8aa3b, v15
	v_exp_f32_e32 v6, v6
	v_mul_f32_e32 v7, 0xbfb8aa3b, v16
	v_add_f32_e32 v5, 1.0, v5
	v_rcp_f32_e32 v5, v5
	v_exp_f32_e32 v7, v7
	v_add_f32_e32 v6, 1.0, v6
	v_rcp_f32_e32 v6, v6
	v_add_f32_e32 v8, -0.5, v5
	v_mul_f32_e32 v5, 0xbfb8aa3b, v17
	v_exp_f32_e32 v5, v5
	v_add_f32_e32 v7, 1.0, v7
	v_add_f32_e32 v6, -0.5, v6
	v_rcp_f32_e32 v7, v7
	v_add_f32_e32 v5, 1.0, v5
	v_rcp_f32_e32 v9, v5
	v_mov_b32_e32 v5, 0
	v_cvt_pk_fp8_f32 v5, v8, v6
	v_add_f32_e32 v6, -0.5, v7
	v_add_f32_e32 v7, -0.5, v9
	v_cvt_pk_fp8_f32 v5, v6, v7 op_sel:[0,0,1]
	ds_write_b128 v100, v[2:5] offset:8192

_Z6k_agg2PK15HIP_vector_typeIjLj2EEPKS_IjLj4EEPKtPKjPf:
	v_lshrrev_b32_e32 v1, 4, v0
	v_lshl_or_b32 v6, s2, 4, v1
	s_mov_b32 s2, 0xc350
	v_cmp_gt_i32_e32 vcc, s2, v6
	s_and_saveexec_b64 s[2:3], vcc
	s_cbranch_execz .LBB3_14
	s_load_dwordx2 s[2:3], s[0:1], 0x18
	s_load_dwordx4 s[4:7], s[0:1], 0x0
	v_lshlrev_b32_e32 v2, 4, v6
	v_and_b32_e32 v48, 15, v0
	v_ashrrev_i32_e32 v3, 31, v2
	v_lshlrev_b32_e32 v12, 2, v48
	s_waitcnt lgkmcnt(0)
	v_lshl_add_u64 v[4:5], v[2:3], 2, s[2:3]
	v_mov_b32_e32 v13, 0
	v_lshl_add_u64 v[4:5], v[4:5], 0, v[12:13]
	global_load_dword v53, v[4:5], off nt
	v_or_b32_e32 v2, v2, v48
	v_ashrrev_i32_e32 v3, 31, v2
	v_lshl_add_u64 v[2:3], v[2:3], 4, s[6:7]
	global_load_dwordx4 v[2:5], v[2:3], off nt
	v_mbcnt_lo_u32_b32 v1, -1, 0
	v_mbcnt_hi_u32_b32 v7, -1, v1
	v_and_b32_e32 v0, 48, v0
	v_and_b32_e32 v49, 64, v7
	v_or_b32_e32 v51, v49, v0
	v_lshlrev_b32_e32 v54, 2, v51
	v_mov_b32_e32 v10, v13
	v_mov_b32_e32 v11, v13
	v_mov_b32_e32 v8, v13
	v_mov_b32_e32 v9, v13
	v_mov_b32_e32 v0, v13
	v_mov_b32_e32 v1, v13
	v_mov_b32_e32 v14, v13
	v_mov_b32_e32 v12, v13
	s_waitcnt vmcnt(1)
	ds_bpermute_b32 v15, v54, v53
	s_waitcnt lgkmcnt(0)
	v_and_b32_e32 v50, 0x7fffffff, v15
	v_min_u32_e32 v16, 24, v50
	v_cmp_lt_i32_e32 vcc, -1, v15
	v_mov_b32_e32 v15, v13
	s_nop 0
	v_cndmask_b32_e32 v52, 0, v16, vcc
	v_cmp_ne_u32_e32 vcc, 0, v52
	s_and_saveexec_b64 s[2:3], vcc
	s_cbranch_execz .LBB3_5
	ds_bpermute_b32 v0, v54, v53 offset:4
	ds_bpermute_b32 v1, v54, v53 offset:8
	s_mov_b32 s8, 0xffff0
	ds_bpermute_b32 v9, v54, v53 offset:12
	ds_bpermute_b32 v16, v54, v53 offset:20
	s_waitcnt lgkmcnt(3)
	v_lshlrev_b32_e32 v8, 4, v0
	v_and_or_b32 v8, v8, s8, v48
	v_lshlrev_b32_e32 v8, 3, v8
	v_bfe_u32 v0, v0, 16, 16
	global_load_dwordx2 v[34:35], v8, s[4:5]
	s_waitcnt lgkmcnt(2)
	v_lshlrev_b32_e32 v8, 4, v1
	v_bfe_u32 v1, v1, 16, 16
	v_lshl_or_b32 v0, v0, 4, v48
	v_lshl_or_b32 v1, v1, 4, v48
	v_lshlrev_b32_e32 v0, 3, v0
	v_and_or_b32 v8, v8, s8, v48
	v_lshlrev_b32_e32 v1, 3, v1
	v_lshlrev_b32_e32 v8, 3, v8
	global_load_dwordx2 v[36:37], v0, s[4:5]
	global_load_dwordx2 v[32:33], v8, s[4:5]
	global_load_dwordx2 v[12:13], v1, s[4:5]
	ds_bpermute_b32 v1, v54, v53 offset:16
	s_waitcnt lgkmcnt(2)
	v_bfe_u32 v8, v9, 16, 16
	v_lshl_or_b32 v8, v8, 4, v48
	ds_bpermute_b32 v17, v54, v53 offset:24
	v_lshlrev_b32_e32 v0, 4, v9
	v_lshlrev_b32_e32 v14, 3, v8
	s_waitcnt lgkmcnt(1)
	v_lshlrev_b32_e32 v8, 4, v1
	v_bfe_u32 v1, v1, 16, 16
	v_and_or_b32 v0, v0, s8, v48
	v_and_or_b32 v8, v8, s8, v48
	v_lshl_or_b32 v1, v1, 4, v48
	v_lshlrev_b32_e32 v0, 3, v0
	v_lshlrev_b32_e32 v15, 3, v8
	v_lshlrev_b32_e32 v1, 3, v1
	global_load_dwordx2 v[30:31], v0, s[4:5]
	global_load_dwordx2 v[10:11], v14, s[4:5]
	global_load_dwordx2 v[8:9], v15, s[4:5]
	s_nop 0
	global_load_dwordx2 v[0:1], v1, s[4:5]
	v_lshlrev_b32_e32 v14, 4, v16
	v_bfe_u32 v15, v16, 16, 16
	v_and_or_b32 v14, v14, s8, v48
	v_lshl_or_b32 v15, v15, 4, v48
	s_waitcnt lgkmcnt(0)
	v_lshlrev_b32_e32 v16, 4, v17
	v_lshlrev_b32_e32 v14, 3, v14
	v_lshlrev_b32_e32 v15, 3, v15
	v_and_or_b32 v16, v16, s8, v48
	v_lshlrev_b32_e32 v16, 3, v16
	global_load_dwordx2 v[22:23], v14, s[4:5]
	global_load_dwordx2 v[18:19], v15, s[4:5]
	s_nop 0
	global_load_dwordx2 v[14:15], v16, s[4:5]
	v_bfe_u32 v17, v17, 16, 16
	v_lshl_or_b32 v17, v17, 4, v48
	v_lshlrev_b32_e32 v17, 3, v17
	global_load_dwordx2 v[24:25], v17, s[4:5]
	ds_bpermute_b32 v16, v54, v53 offset:28
	v_cmp_lt_u32_e32 vcc, 16, v52
	s_waitcnt lgkmcnt(0)
	v_lshlrev_b32_e32 v17, 4, v16
	v_and_or_b32 v17, v17, s8, v48
	v_lshlrev_b32_e32 v17, 3, v17
	global_load_dwordx2 v[28:29], v17, s[4:5]
	ds_bpermute_b32 v17, v54, v53 offset:32
	v_bfe_u32 v16, v16, 16, 16
	v_lshl_or_b32 v16, v16, 4, v48
	v_lshlrev_b32_e32 v16, 3, v16
	s_waitcnt lgkmcnt(0)
	v_lshlrev_b32_e32 v20, 4, v17
	v_bfe_u32 v17, v17, 16, 16
	v_and_or_b32 v20, v20, s8, v48
	v_lshl_or_b32 v17, v17, 4, v48
	v_lshlrev_b32_e32 v20, 3, v20
	v_lshlrev_b32_e32 v17, 3, v17
	global_load_dwordx2 v[26:27], v16, s[4:5]
	s_nop 0
	global_load_dwordx2 v[20:21], v20, s[4:5]
	s_nop 0
	global_load_dwordx2 v[16:17], v17, s[4:5]
	s_waitcnt vmcnt(15)
	v_cvt_pk_f32_fp8_e32 v[38:39], v34
	v_cvt_pk_f32_fp8_sdwa v[42:43], v34 src0_sel:WORD_1
	v_cvt_pk_f32_fp8_e32 v[44:45], v35
	v_cvt_pk_f32_fp8_sdwa v[34:35], v35 src0_sel:WORD_1
	s_waitcnt vmcnt(14)
	v_cvt_pk_f32_fp8_sdwa v[58:59], v36 src0_sel:WORD_1
	v_cvt_pk_f32_fp8_e32 v[56:57], v36
	v_cvt_pk_f32_fp8_e32 v[60:61], v37
	v_cvt_pk_f32_fp8_sdwa v[62:63], v37 src0_sel:WORD_1
	s_waitcnt vmcnt(13)
	v_cvt_pk_f32_fp8_e32 v[46:47], v32
	v_pk_add_f32 v[36:37], v[38:39], 0 op_sel_hi:[1,0]
	v_pk_add_f32 v[38:39], v[42:43], 0 op_sel_hi:[1,0]
	v_pk_add_f32 v[56:57], v[36:37], v[56:57]
	v_pk_add_f32 v[42:43], v[38:39], v[58:59]
	s_waitcnt vmcnt(12)
	v_cvt_pk_f32_fp8_e32 v[58:59], v12
	v_pk_add_f32 v[38:39], v[44:45], 0 op_sel_hi:[1,0]
	v_pk_add_f32 v[46:47], v[56:57], v[46:47]
	v_pk_add_f32 v[38:39], v[38:39], v[60:61]
	s_waitcnt vmcnt(11)
	v_cvt_pk_f32_fp8_e32 v[60:61], v30
	s_waitcnt vmcnt(10)
	v_cvt_pk_f32_fp8_e32 v[56:57], v10
	v_pk_add_f32 v[46:47], v[46:47], v[58:59]
	s_waitcnt vmcnt(9)
	v_cvt_pk_f32_fp8_e32 v[58:59], v8
	v_pk_add_f32 v[46:47], v[46:47], v[60:61]
	s_waitcnt vmcnt(8)
	v_cvt_pk_f32_fp8_e32 v[60:61], v0
	v_pk_add_f32 v[46:47], v[46:47], v[56:57]
	v_cvt_pk_f32_fp8_sdwa v[40:41], v32 src0_sel:WORD_1
	v_pk_add_f32 v[46:47], v[46:47], v[58:59]
	v_cvt_pk_f32_fp8_sdwa v[44:45], v12 src0_sel:WORD_1
	v_pk_add_f32 v[46:47], v[46:47], v[60:61]
	v_pk_add_f32 v[40:41], v[42:43], v[40:41]
	s_waitcnt vmcnt(7)
	v_cvt_pk_f32_fp8_e32 v[56:57], v22
	s_waitcnt vmcnt(6)
	v_cvt_pk_f32_fp8_e32 v[58:59], v18
	s_waitcnt vmcnt(5)
	v_cvt_pk_f32_fp8_e32 v[60:61], v14
	v_cvt_pk_f32_fp8_sdwa v[42:43], v10 src0_sel:WORD_1
	v_pk_add_f32 v[46:47], v[46:47], v[56:57]
	v_cvt_pk_f32_fp8_e32 v[56:57], v13
	v_pk_add_f32 v[46:47], v[46:47], v[58:59]
	s_waitcnt vmcnt(4)
	v_cvt_pk_f32_fp8_e32 v[58:59], v24
	v_pk_add_f32 v[60:61], v[46:47], v[60:61]
	v_cvt_pk_f32_fp8_sdwa v[46:47], v13 src0_sel:WORD_1
	v_pk_add_f32 v[40:41], v[40:41], v[44:45]
	v_pk_add_f32 v[12:13], v[60:61], v[58:59]
	v_cvt_pk_f32_fp8_sdwa v[58:59], v30 src0_sel:WORD_1
	v_cvt_pk_f32_fp8_sdwa v[44:45], v8 src0_sel:WORD_1
	v_cvt_pk_f32_fp8_e32 v[36:37], v33
	v_cvt_pk_f32_fp8_sdwa v[32:33], v33 src0_sel:WORD_1
	v_pk_add_f32 v[40:41], v[40:41], v[58:59]
	v_cvt_pk_f32_fp8_sdwa v[58:59], v0 src0_sel:WORD_1
	v_pk_add_f32 v[40:41], v[40:41], v[42:43]
	v_cvt_pk_f32_fp8_sdwa v[42:43], v22 src0_sel:WORD_1
	v_pk_add_f32 v[40:41], v[40:41], v[44:45]
	v_cvt_pk_f32_fp8_sdwa v[44:45], v18 src0_sel:WORD_1
	v_pk_add_f32 v[40:41], v[40:41], v[58:59]
	v_pk_add_f32 v[34:35], v[34:35], 0 op_sel_hi:[1,0]
	v_pk_add_f32 v[40:41], v[40:41], v[42:43]
	v_cvt_pk_f32_fp8_sdwa v[42:43], v14 src0_sel:WORD_1
	v_pk_add_f32 v[40:41], v[40:41], v[44:45]
	v_cvt_pk_f32_fp8_sdwa v[44:45], v24 src0_sel:WORD_1
	v_cvt_pk_f32_fp8_e32 v[60:61], v31
	v_pk_add_f32 v[40:41], v[40:41], v[42:43]
	s_waitcnt vmcnt(3)
	v_cvt_pk_f32_fp8_sdwa v[42:43], v28 src0_sel:WORD_1
	v_cvt_pk_f32_fp8_sdwa v[30:31], v31 src0_sel:WORD_1
	v_pk_add_f32 v[34:35], v[34:35], v[62:63]
	v_cvt_pk_f32_fp8_e32 v[58:59], v11
	v_cvt_pk_f32_fp8_sdwa v[10:11], v11 src0_sel:WORD_1
	v_pk_add_f32 v[40:41], v[40:41], v[44:45]
	v_cvt_pk_f32_fp8_e32 v[44:45], v9
	v_cvt_pk_f32_fp8_sdwa v[8:9], v9 src0_sel:WORD_1
	v_pk_add_f32 v[32:33], v[34:35], v[32:33]
	v_pk_add_f32 v[40:41], v[40:41], v[42:43]
	v_cvt_pk_f32_fp8_e32 v[42:43], v1
	v_cvt_pk_f32_fp8_sdwa v[0:1], v1 src0_sel:WORD_1
	v_pk_add_f32 v[32:33], v[32:33], v[46:47]
	v_pk_add_f32 v[36:37], v[38:39], v[36:37]
	v_cvt_pk_f32_fp8_e32 v[38:39], v23
	v_cvt_pk_f32_fp8_sdwa v[22:23], v23 src0_sel:WORD_1
	v_pk_add_f32 v[30:31], v[32:33], v[30:31]
	v_pk_add_f32 v[36:37], v[36:37], v[56:57]
	v_cvt_pk_f32_fp8_e32 v[56:57], v19
	v_cvt_pk_f32_fp8_sdwa v[18:19], v19 src0_sel:WORD_1
	v_pk_add_f32 v[10:11], v[30:31], v[10:11]
	v_pk_add_f32 v[36:37], v[36:37], v[60:61]
	v_cvt_pk_f32_fp8_e32 v[60:61], v15
	v_cvt_pk_f32_fp8_sdwa v[14:15], v15 src0_sel:WORD_1
	v_pk_add_f32 v[8:9], v[10:11], v[8:9]
	v_pk_add_f32 v[36:37], v[36:37], v[58:59]
	v_cvt_pk_f32_fp8_e32 v[58:59], v25
	v_cvt_pk_f32_fp8_sdwa v[24:25], v25 src0_sel:WORD_1
	v_pk_add_f32 v[0:1], v[8:9], v[0:1]
	v_cvt_pk_f32_fp8_e32 v[62:63], v28
	v_pk_add_f32 v[36:37], v[36:37], v[44:45]
	v_cvt_pk_f32_fp8_e32 v[44:45], v29
	v_cvt_pk_f32_fp8_sdwa v[28:29], v29 src0_sel:WORD_1
	v_pk_add_f32 v[0:1], v[0:1], v[22:23]
	s_waitcnt vmcnt(1)
	v_cvt_pk_f32_fp8_e32 v[10:11], v20
	v_pk_add_f32 v[0:1], v[0:1], v[18:19]
	v_pk_add_f32 v[36:37], v[36:37], v[42:43]
	v_pk_add_f32 v[0:1], v[0:1], v[14:15]
	v_cvt_pk_f32_fp8_sdwa v[8:9], v26 src0_sel:WORD_1
	v_pk_add_f32 v[0:1], v[0:1], v[24:25]
	v_pk_add_f32 v[12:13], v[12:13], v[62:63]
	v_pk_add_f32 v[14:15], v[0:1], v[28:29]
	v_cvt_pk_f32_fp8_e32 v[0:1], v26
	s_waitcnt vmcnt(0)
	v_cvt_pk_f32_fp8_e32 v[28:29], v16
	v_pk_add_f32 v[36:37], v[36:37], v[38:39]
	v_cvt_pk_f32_fp8_sdwa v[22:23], v27 src0_sel:WORD_1
	v_cvt_pk_f32_fp8_sdwa v[24:25], v20 src0_sel:WORD_1
	v_pk_add_f32 v[36:37], v[36:37], v[56:57]
	v_cvt_pk_f32_fp8_e32 v[18:19], v27
	v_cvt_pk_f32_fp8_e32 v[26:27], v21
	v_cvt_pk_f32_fp8_sdwa v[20:21], v21 src0_sel:WORD_1
	v_cvt_pk_f32_fp8_sdwa v[30:31], v16 src0_sel:WORD_1
	v_pk_add_f32 v[0:1], v[12:13], v[0:1]
	v_pk_add_f32 v[36:37], v[36:37], v[60:61]
	v_cvt_pk_f32_fp8_e32 v[32:33], v17
	v_cvt_pk_f32_fp8_sdwa v[16:17], v17 src0_sel:WORD_1
	v_pk_add_f32 v[0:1], v[0:1], v[10:11]
	v_pk_add_f32 v[36:37], v[36:37], v[58:59]
	v_pk_add_f32 v[10:11], v[0:1], v[28:29]
	v_pk_add_f32 v[0:1], v[40:41], v[8:9]
	v_pk_add_f32 v[36:37], v[36:37], v[44:45]
	v_pk_add_f32 v[0:1], v[0:1], v[24:25]
	v_pk_add_f32 v[12:13], v[14:15], v[22:23]
	v_pk_add_f32 v[8:9], v[0:1], v[30:31]
	v_pk_add_f32 v[0:1], v[36:37], v[18:19]
	v_pk_add_f32 v[12:13], v[12:13], v[20:21]
	v_pk_add_f32 v[0:1], v[0:1], v[26:27]
	v_pk_add_f32 v[12:13], v[12:13], v[16:17]
	v_pk_add_f32 v[0:1], v[0:1], v[32:33]
	v_mov_b32_e32 v15, v13
	v_mov_b32_e32 v14, v12
	s_and_saveexec_b64 s[6:7], vcc
	s_cbranch_execz .LBB3_4
	ds_bpermute_b32 v14, v54, v53 offset:36
	ds_bpermute_b32 v15, v54, v53 offset:40
	ds_bpermute_b32 v16, v54, v53 offset:44
	s_waitcnt lgkmcnt(2)
	v_lshlrev_b32_e32 v17, 4, v14
	v_bfe_u32 v14, v14, 16, 16
	v_and_or_b32 v17, v17, s8, v48
	v_lshl_or_b32 v14, v14, 4, v48
	v_lshlrev_b32_e32 v17, 3, v17
	v_lshlrev_b32_e32 v14, 3, v14
	global_load_dwordx2 v[20:21], v17, s[4:5]
	global_load_dwordx2 v[22:23], v14, s[4:5]
	s_waitcnt lgkmcnt(1)
	v_lshlrev_b32_e32 v14, 4, v15
	v_and_or_b32 v14, v14, s8, v48
	v_lshlrev_b32_e32 v14, 3, v14
	global_load_dwordx2 v[24:25], v14, s[4:5]
	v_bfe_u32 v14, v15, 16, 16
	s_waitcnt lgkmcnt(0)
	v_bfe_u32 v15, v16, 16, 16
	v_lshl_or_b32 v14, v14, 4, v48
	v_lshl_or_b32 v15, v15, 4, v48
	v_lshlrev_b32_e32 v14, 3, v14
	v_lshlrev_b32_e32 v15, 3, v15
	global_load_dwordx2 v[26:27], v14, s[4:5]
	global_load_dwordx2 v[18:19], v15, s[4:5]
	v_lshlrev_b32_e32 v14, 4, v16
	v_and_or_b32 v14, v14, s8, v48
	v_lshlrev_b32_e32 v14, 3, v14
	global_load_dwordx2 v[28:29], v14, s[4:5]
	ds_bpermute_b32 v14, v54, v53 offset:48
	s_waitcnt lgkmcnt(0)
	v_lshlrev_b32_e32 v15, 4, v14
	v_and_or_b32 v15, v15, s8, v48
	v_bfe_u32 v14, v14, 16, 16
	v_lshlrev_b32_e32 v15, 3, v15
	v_lshl_or_b32 v14, v14, 4, v48
	global_load_dwordx2 v[16:17], v15, s[4:5]
	v_lshlrev_b32_e32 v14, 3, v14
	global_load_dwordx2 v[14:15], v14, s[4:5]
	s_waitcnt vmcnt(7)
	v_cvt_pk_f32_fp8_e32 v[30:31], v20
	v_cvt_pk_f32_fp8_sdwa v[32:33], v20 src0_sel:WORD_1
	v_cvt_pk_f32_fp8_e32 v[34:35], v21
	v_cvt_pk_f32_fp8_sdwa v[20:21], v21 src0_sel:WORD_1
	s_waitcnt vmcnt(6)
	v_cvt_pk_f32_fp8_e32 v[36:37], v22
	v_cvt_pk_f32_fp8_sdwa v[38:39], v22 src0_sel:WORD_1
	v_cvt_pk_f32_fp8_e32 v[40:41], v23
	v_cvt_pk_f32_fp8_sdwa v[22:23], v23 src0_sel:WORD_1
	s_waitcnt vmcnt(5)
	v_cvt_pk_f32_fp8_e32 v[42:43], v24
	v_cvt_pk_f32_fp8_sdwa v[44:45], v24 src0_sel:WORD_1
	v_cvt_pk_f32_fp8_e32 v[46:47], v25
	v_cvt_pk_f32_fp8_sdwa v[24:25], v25 src0_sel:WORD_1
	s_waitcnt vmcnt(4)
	v_cvt_pk_f32_fp8_e32 v[54:55], v26
	v_cvt_pk_f32_fp8_sdwa v[56:57], v26 src0_sel:WORD_1
	v_cvt_pk_f32_fp8_e32 v[58:59], v27
	v_cvt_pk_f32_fp8_sdwa v[26:27], v27 src0_sel:WORD_1
	v_pk_add_f32 v[10:11], v[10:11], v[30:31]
	s_waitcnt vmcnt(2)
	v_cvt_pk_f32_fp8_e32 v[60:61], v28
	v_cvt_pk_f32_fp8_sdwa v[30:31], v28 src0_sel:WORD_1
	v_pk_add_f32 v[8:9], v[8:9], v[32:33]
	v_cvt_pk_f32_fp8_e32 v[32:33], v29
	v_cvt_pk_f32_fp8_sdwa v[28:29], v29 src0_sel:WORD_1
	v_pk_add_f32 v[12:13], v[12:13], v[20:21]
	v_pk_add_f32 v[0:1], v[0:1], v[34:35]
	v_cvt_pk_f32_fp8_e32 v[34:35], v18
	v_cvt_pk_f32_fp8_sdwa v[20:21], v18 src0_sel:WORD_1
	v_pk_add_f32 v[10:11], v[10:11], v[36:37]
	v_cvt_pk_f32_fp8_e32 v[36:37], v19
	v_cvt_pk_f32_fp8_sdwa v[18:19], v19 src0_sel:WORD_1
	v_pk_add_f32 v[12:13], v[12:13], v[22:23]
	v_pk_add_f32 v[8:9], v[8:9], v[38:39]
	s_waitcnt vmcnt(1)
	v_cvt_pk_f32_fp8_e32 v[38:39], v16
	v_pk_add_f32 v[0:1], v[0:1], v[40:41]
	v_cvt_pk_f32_fp8_sdwa v[40:41], v16 src0_sel:WORD_1
	v_cvt_pk_f32_fp8_e32 v[22:23], v17
	v_cvt_pk_f32_fp8_sdwa v[16:17], v17 src0_sel:WORD_1
	v_pk_add_f32 v[12:13], v[12:13], v[24:25]
	v_pk_add_f32 v[10:11], v[10:11], v[42:43]
	s_waitcnt vmcnt(0)
	v_cvt_pk_f32_fp8_e32 v[42:43], v14
	v_pk_add_f32 v[8:9], v[8:9], v[44:45]
	v_cvt_pk_f32_fp8_sdwa v[44:45], v14 src0_sel:WORD_1
	v_pk_add_f32 v[0:1], v[0:1], v[46:47]
	v_cvt_pk_f32_fp8_e32 v[46:47], v15
	v_cvt_pk_f32_fp8_sdwa v[14:15], v15 src0_sel:WORD_1
	v_pk_add_f32 v[12:13], v[12:13], v[26:27]
	v_pk_add_f32 v[10:11], v[10:11], v[54:55]
	v_pk_add_f32 v[8:9], v[8:9], v[56:57]
	v_pk_add_f32 v[0:1], v[0:1], v[58:59]
	v_pk_add_f32 v[12:13], v[12:13], v[28:29]
	v_pk_add_f32 v[10:11], v[10:11], v[60:61]
	v_pk_add_f32 v[8:9], v[8:9], v[30:31]
	v_pk_add_f32 v[0:1], v[0:1], v[32:33]
	v_pk_add_f32 v[12:13], v[12:13], v[18:19]
	v_pk_add_f32 v[10:11], v[10:11], v[34:35]
	v_pk_add_f32 v[8:9], v[8:9], v[20:21]
	v_pk_add_f32 v[0:1], v[0:1], v[36:37]
	v_pk_add_f32 v[12:13], v[12:13], v[16:17]
	v_pk_add_f32 v[10:11], v[10:11], v[38:39]
	v_pk_add_f32 v[8:9], v[8:9], v[40:41]
	v_pk_add_f32 v[0:1], v[0:1], v[22:23]
	v_pk_add_f32 v[14:15], v[12:13], v[14:15]
	v_pk_add_f32 v[10:11], v[10:11], v[42:43]
	v_pk_add_f32 v[8:9], v[8:9], v[44:45]
	v_pk_add_f32 v[0:1], v[0:1], v[46:47]
	v_mov_b64_e32 v[12:13], v[14:15]
